# baseline (speedup 1.0000x reference)
.Lp_main:
	s_load_dwordx2 s[10:11], s[0:1], 0x0
	s_load_dwordx4 s[12:15], s[0:1], 0x10
	s_load_dwordx2 s[16:17], s[0:1], 0x20
	s_load_dwordx4 s[20:23], s[0:1], 0x28
	v_readfirstlane_b32 s3, v0
	v_and_b32_e32 v154, 63, v0
	v_lshrrev_b32_e32 v155, 5, v154
	v_lshlrev_b32_e32 v156, 4, v0
	v_lshlrev_b32_e32 v157, 4, v154
	v_lshlrev_b32_e32 v158, 8, v1
	v_lshl_add_u32 v158, v155, 5, v158
	v_lshlrev_b32_e32 v159, 4, v155
	v_lshrrev_b32_e32 v160, 3, v0
	v_lshlrev_b32_e32 v160, 12, v160
	v_and_b32_e32 v161, 7, v0
	v_lshl_add_u32 v160, v161, 4, v160
	s_lshr_b32 s41, s2, 3
	s_and_b32 s42, s2, 7
	s_lshl_b32 s24, s42, 2
	s_bfe_u32 s25, s2, 0x20003
	s_add_u32 s24, s24, s25
	s_lshr_b32 s25, s2, 5
	s_lshr_b32 s26, s3, 6
	s_lshl_b32 s27, s25, 2
	s_add_u32 s27, s27, s26
	s_mov_b32 s4, 0x4038aa3b
	s_mov_b32 s5, s4
	s_lshl_b32 s40, s26, 6
	s_waitcnt lgkmcnt(0)
	s_lshl_b32 s28, s24, 15
	s_add_u32 s28, s28, 0x1000
	s_add_u32 s10, s10, s28
	s_addc_u32 s11, s11, 0
	s_lshl_b32 s34, s41, 17
	s_lshl_b32 s35, s42, 9
	s_add_u32 s34, s34, s35
	s_add_u32 s34, s14, s34
	s_addc_u32 s35, s15, 0
	s_lshl_b32 s28, s27, 13
	s_add_u32 s28, s8, s28
	s_addc_u32 s29, s9, 0
	s_lshl_b32 s30, s27, 7
	s_add_u32 s30, s12, s30
	s_addc_u32 s31, s13, 0
	s_cmp_eq_u32 s26, 1
	s_cbranch_scc0 .Lp_wl2
	global_load_dword v162, v158, s[28:29]
.Lp_wl2:
	s_cmp_eq_u32 s26, 2
	s_cbranch_scc0 .Lp_wl0
	global_load_dword v162, v160, s[34:35]
.Lp_wl0:
	global_load_dwordx4 v[2:5], v156, s[10:11] offset:-4096
	global_load_dwordx4 v[6:9], v156, s[10:11] offset:0
	s_add_u32 s10, s10, 0x2000
	s_addc_u32 s11, s11, 0
	global_load_dwordx4 v[10:13], v156, s[10:11] offset:-4096
	global_load_dwordx4 v[14:17], v156, s[10:11] offset:0
	s_add_u32 s10, s10, 0x2000
	s_addc_u32 s11, s11, 0
	global_load_dwordx4 v[18:21], v156, s[10:11] offset:-4096
	global_load_dwordx4 v[22:25], v156, s[10:11] offset:0
	s_add_u32 s10, s10, 0x2000
	s_addc_u32 s11, s11, 0
	global_load_dwordx4 v[26:29], v156, s[10:11] offset:-4096
	global_load_dwordx4 v[30:33], v156, s[10:11] offset:0
	global_load_dwordx4 v[34:37], v158, s[28:29] offset:0
	global_load_dwordx4 v[38:41], v158, s[28:29] offset:16
	global_load_dwordx4 v[42:45], v158, s[28:29] offset:64
	global_load_dwordx4 v[46:49], v158, s[28:29] offset:80
	global_load_dwordx4 v[50:53], v158, s[28:29] offset:128
	global_load_dwordx4 v[54:57], v158, s[28:29] offset:144
	global_load_dwordx4 v[58:61], v158, s[28:29] offset:192
	global_load_dwordx4 v[62:65], v158, s[28:29] offset:208
	global_load_dwordx4 v[66:69], v159, s[30:31] offset:0
	global_load_dwordx4 v[70:73], v159, s[30:31] offset:32
	global_load_dwordx4 v[74:77], v159, s[30:31] offset:64
	global_load_dwordx4 v[78:81], v159, s[30:31] offset:96
	global_load_dwordx4 v[168:171], v160, s[34:35] offset:0
	global_load_dwordx4 v[172:175], v160, s[34:35] offset:128
	global_load_dwordx4 v[176:179], v160, s[34:35] offset:256
	global_load_dwordx4 v[180:183], v160, s[34:35] offset:384
	v_bfe_u32 v163, v0, 1, 3
	v_mul_u32_u24_e32 v163, 0x210, v163
	v_lshrrev_b32_e32 v164, 4, v0
	v_lshl_add_u32 v163, v164, 4, v163
	v_and_b32_e32 v164, 1, v0
	v_lshl_add_u32 v163, v164, 3, v163
	v_lshrrev_b32_e32 v164, 3, v0
	v_mul_u32_u24_e32 v164, 0x110, v164
	v_lshl_add_u32 v164, v161, 3, v164
	v_add_u32_e32 v164, 0x4200, v164
	v_mul_u32_u24_e32 v165, 0x210, v155
	v_lshl_add_u32 v165, v1, 4, v165
	v_mul_u32_u24_e32 v166, 0x110, v1
	v_lshl_add_u32 v166, v155, 4, v166
	v_add_u32_e32 v166, s40, v166
	v_add_u32_e32 v166, 0x4200, v166
	v_mul_u32_u24_e32 v167, 0x880, v155
	v_lshl_add_u32 v167, v1, 1, v167
	v_add_u32_e32 v167, s40, v167
	v_add_u32_e32 v167, 0x4200, v167
	s_lshl_b32 s32, s24, 18
	s_lshl_b32 s33, s27, 11
	s_add_u32 s32, s32, s33
	s_add_u32 s32, s16, s32
	s_addc_u32 s33, s17, 0
	s_lshl_b32 s36, s41, 16
	s_lshl_b32 s37, s42, 13
	s_add_u32 s36, s36, s37
	s_lshl_b32 s37, s26, 11
	s_add_u32 s36, s36, s37
	s_add_u32 s36, s20, s36
	s_addc_u32 s37, s21, 0
	s_lshl_b32 s38, s42, 18
	s_lshl_b32 s39, s26, 16
	s_add_u32 s38, s38, s39
	s_lshl_b32 s39, s41, 11
	s_add_u32 s38, s38, s39
	s_add_u32 s38, s22, s38
	s_addc_u32 s39, s23, 0
	s_waitcnt vmcnt(23)
	v_cvt_pk_f16_f32 v2, v2, v3
	v_cvt_pk_f16_f32 v3, v4, v5
	ds_write_b64 v163, v[2:3] offset:0
	s_waitcnt vmcnt(22)
	v_cvt_pk_f16_f32 v6, v6, v7
	v_cvt_pk_f16_f32 v7, v8, v9
	ds_write_b64 v163, v[6:7] offset:256
	s_waitcnt vmcnt(21)
	v_cvt_pk_f16_f32 v10, v10, v11
	v_cvt_pk_f16_f32 v11, v12, v13
	ds_write_b64 v163, v[10:11] offset:4224
	s_waitcnt vmcnt(20)
	v_cvt_pk_f16_f32 v14, v14, v15
	v_cvt_pk_f16_f32 v15, v16, v17
	ds_write_b64 v163, v[14:15] offset:4480
	s_waitcnt vmcnt(19)
	v_cvt_pk_f16_f32 v18, v18, v19
	v_cvt_pk_f16_f32 v19, v20, v21
	ds_write_b64 v163, v[18:19] offset:8448
	s_waitcnt vmcnt(18)
	v_cvt_pk_f16_f32 v22, v22, v23
	v_cvt_pk_f16_f32 v23, v24, v25
	ds_write_b64 v163, v[22:23] offset:8704
	s_waitcnt vmcnt(17)
	v_cvt_pk_f16_f32 v26, v26, v27
	v_cvt_pk_f16_f32 v27, v28, v29
	ds_write_b64 v163, v[26:27] offset:12672
	s_waitcnt vmcnt(16)
	v_cvt_pk_f16_f32 v30, v30, v31
	v_cvt_pk_f16_f32 v31, v32, v33
	ds_write_b64 v163, v[30:31] offset:12928
	s_waitcnt lgkmcnt(0)
	s_barrier
	ds_read_b128 v[2:5], v165 offset:0
	ds_read_b128 v[6:9], v165 offset:1056
	ds_read_b128 v[10:13], v165 offset:2112
	ds_read_b128 v[14:17], v165 offset:3168
	ds_read_b128 v[18:21], v165 offset:4224
	ds_read_b128 v[22:25], v165 offset:5280
	ds_read_b128 v[26:29], v165 offset:6336
	ds_read_b128 v[30:33], v165 offset:7392
	s_waitcnt vmcnt(8)
	v_cvt_pk_f16_f32 v82, v34, v35
	v_cvt_pk_f16_f32 v83, v36, v37
	v_cvt_pk_f16_f32 v84, v38, v39
	v_cvt_pk_f16_f32 v85, v40, v41
	v_cvt_pk_f16_f32 v86, v42, v43
	v_cvt_pk_f16_f32 v87, v44, v45
	v_cvt_pk_f16_f32 v88, v46, v47
	v_cvt_pk_f16_f32 v89, v48, v49
	v_cvt_pk_f16_f32 v90, v50, v51
	v_cvt_pk_f16_f32 v91, v52, v53
	v_cvt_pk_f16_f32 v92, v54, v55
	v_cvt_pk_f16_f32 v93, v56, v57
	v_cvt_pk_f16_f32 v94, v58, v59
	v_cvt_pk_f16_f32 v95, v60, v61
	v_cvt_pk_f16_f32 v96, v62, v63
	v_cvt_pk_f16_f32 v97, v64, v65
	ds_read_b128 v[34:37], v165 offset:8448
	ds_read_b128 v[38:41], v165 offset:9504
	ds_read_b128 v[42:45], v165 offset:10560
	ds_read_b128 v[46:49], v165 offset:11616
	s_waitcnt vmcnt(4)
	v_pk_mul_f32 v[66:67], v[66:67], s[4:5] op_sel_hi:[1,0]
	v_pk_mul_f32 v[68:69], v[68:69], s[4:5] op_sel_hi:[1,0]
	v_pk_mul_f32 v[70:71], v[70:71], s[4:5] op_sel_hi:[1,0]
	v_pk_mul_f32 v[72:73], v[72:73], s[4:5] op_sel_hi:[1,0]
	v_pk_mul_f32 v[74:75], v[74:75], s[4:5] op_sel_hi:[1,0]
	v_pk_mul_f32 v[76:77], v[76:77], s[4:5] op_sel_hi:[1,0]
	v_pk_mul_f32 v[78:79], v[78:79], s[4:5] op_sel_hi:[1,0]
	v_pk_mul_f32 v[80:81], v[80:81], s[4:5] op_sel_hi:[1,0]
	s_waitcnt lgkmcnt(8)
	v_mfma_f32_32x32x16_f16 v[98:113], v[82:85], v[2:5], 0
	v_mfma_f32_32x32x16_f16 v[98:113], v[86:89], v[6:9], v[98:113]
	v_mfma_f32_32x32x16_f16 v[98:113], v[90:93], v[10:13], v[98:113]
	v_mfma_f32_32x32x16_f16 v[98:113], v[94:97], v[14:17], v[98:113]
	ds_read_b128 v[50:53], v165 offset:12672
	ds_read_b128 v[54:57], v165 offset:13728
	ds_read_b128 v[58:61], v165 offset:14784
	ds_read_b128 v[62:65], v165 offset:15840
	s_waitcnt lgkmcnt(8)
	v_mfma_f32_32x32x16_f16 v[114:129], v[82:85], v[18:21], 0
	v_mfma_f32_32x32x16_f16 v[114:129], v[86:89], v[22:25], v[114:129]
	v_mfma_f32_32x32x16_f16 v[114:129], v[90:93], v[26:29], v[114:129]
	v_mfma_f32_32x32x16_f16 v[114:129], v[94:97], v[30:33], v[114:129]
	s_nop 7
	v_pk_fma_f32 v[130:131], v[98:99], s[4:5], v[66:67] op_sel_hi:[1,0,1]
	v_pk_fma_f32 v[132:133], v[100:101], s[4:5], v[68:69] op_sel_hi:[1,0,1]
	v_pk_fma_f32 v[134:135], v[102:103], s[4:5], v[70:71] op_sel_hi:[1,0,1]
	v_pk_fma_f32 v[136:137], v[104:105], s[4:5], v[72:73] op_sel_hi:[1,0,1]
	v_pk_fma_f32 v[138:139], v[106:107], s[4:5], v[74:75] op_sel_hi:[1,0,1]
	v_pk_fma_f32 v[140:141], v[108:109], s[4:5], v[76:77] op_sel_hi:[1,0,1]
	v_pk_fma_f32 v[142:143], v[110:111], s[4:5], v[78:79] op_sel_hi:[1,0,1]
	v_pk_fma_f32 v[144:145], v[112:113], s[4:5], v[80:81] op_sel_hi:[1,0,1]
	v_exp_f32_e32 v130, v130
	v_exp_f32_e32 v131, v131
	v_exp_f32_e32 v132, v132
	v_exp_f32_e32 v133, v133
	v_exp_f32_e32 v134, v134
	v_exp_f32_e32 v135, v135
	v_exp_f32_e32 v136, v136
	v_exp_f32_e32 v137, v137
	v_exp_f32_e32 v138, v138
	v_exp_f32_e32 v139, v139
	v_exp_f32_e32 v140, v140
	v_exp_f32_e32 v141, v141
	v_exp_f32_e32 v142, v142
	v_exp_f32_e32 v143, v143
	v_exp_f32_e32 v144, v144
	v_exp_f32_e32 v145, v145
	v_pk_add_f32 v[130:131], v[130:131], 1.0 op_sel_hi:[1,0]
	v_pk_add_f32 v[132:133], v[132:133], 1.0 op_sel_hi:[1,0]
	v_pk_add_f32 v[134:135], v[134:135], 1.0 op_sel_hi:[1,0]
	v_pk_add_f32 v[136:137], v[136:137], 1.0 op_sel_hi:[1,0]
	v_pk_add_f32 v[138:139], v[138:139], 1.0 op_sel_hi:[1,0]
	v_pk_add_f32 v[140:141], v[140:141], 1.0 op_sel_hi:[1,0]
	v_pk_add_f32 v[142:143], v[142:143], 1.0 op_sel_hi:[1,0]
	v_pk_add_f32 v[144:145], v[144:145], 1.0 op_sel_hi:[1,0]
	v_rcp_f32_e32 v130, v130
	v_rcp_f32_e32 v131, v131
	v_rcp_f32_e32 v132, v132
	v_rcp_f32_e32 v133, v133
	v_rcp_f32_e32 v134, v134
	v_rcp_f32_e32 v135, v135
	v_rcp_f32_e32 v136, v136
	v_rcp_f32_e32 v137, v137
	v_rcp_f32_e32 v138, v138
	v_rcp_f32_e32 v139, v139
	v_rcp_f32_e32 v140, v140
	v_rcp_f32_e32 v141, v141
	v_rcp_f32_e32 v142, v142
	v_rcp_f32_e32 v143, v143
	v_rcp_f32_e32 v144, v144
	v_rcp_f32_e32 v145, v145
	v_pk_fma_f32 v[130:131], v[130:131], 2.0, 1.0 op_sel_hi:[1,0,0] neg_lo:[1,0,0] neg_hi:[1,0,0]
	v_pk_fma_f32 v[132:133], v[132:133], 2.0, 1.0 op_sel_hi:[1,0,0] neg_lo:[1,0,0] neg_hi:[1,0,0]
	v_pk_fma_f32 v[134:135], v[134:135], 2.0, 1.0 op_sel_hi:[1,0,0] neg_lo:[1,0,0] neg_hi:[1,0,0]
	v_pk_fma_f32 v[136:137], v[136:137], 2.0, 1.0 op_sel_hi:[1,0,0] neg_lo:[1,0,0] neg_hi:[1,0,0]
	v_pk_fma_f32 v[138:139], v[138:139], 2.0, 1.0 op_sel_hi:[1,0,0] neg_lo:[1,0,0] neg_hi:[1,0,0]
	v_pk_fma_f32 v[140:141], v[140:141], 2.0, 1.0 op_sel_hi:[1,0,0] neg_lo:[1,0,0] neg_hi:[1,0,0]
	v_pk_fma_f32 v[142:143], v[142:143], 2.0, 1.0 op_sel_hi:[1,0,0] neg_lo:[1,0,0] neg_hi:[1,0,0]
	v_pk_fma_f32 v[144:145], v[144:145], 2.0, 1.0 op_sel_hi:[1,0,0] neg_lo:[1,0,0] neg_hi:[1,0,0]
	v_cvt_pk_f16_f32 v146, v130, v131
	v_cvt_pk_f16_f32 v147, v132, v133
	v_cvt_pk_f16_f32 v148, v134, v135
	v_cvt_pk_f16_f32 v149, v136, v137
	v_cvt_pk_f16_f32 v150, v138, v139
	v_cvt_pk_f16_f32 v151, v140, v141
	v_cvt_pk_f16_f32 v152, v142, v143
	v_cvt_pk_f16_f32 v153, v144, v145
	s_nop 1
	v_permlane32_swap_b32_e32 v146, v148
	v_permlane32_swap_b32_e32 v147, v149
	v_permlane32_swap_b32_e32 v150, v152
	v_permlane32_swap_b32_e32 v151, v153
	global_store_dwordx4 v157, v[146:149], s[32:33] sc1
	global_store_dwordx4 v157, v[150:153], s[32:33] offset:1024 sc1
	s_add_u32 s32, s32, 0x10000
	s_addc_u32 s33, s33, 0
	s_waitcnt lgkmcnt(4)
	v_mfma_f32_32x32x16_f16 v[98:113], v[82:85], v[34:37], 0
	v_mfma_f32_32x32x16_f16 v[98:113], v[86:89], v[38:41], v[98:113]
	v_mfma_f32_32x32x16_f16 v[98:113], v[90:93], v[42:45], v[98:113]
	v_mfma_f32_32x32x16_f16 v[98:113], v[94:97], v[46:49], v[98:113]
	v_pk_fma_f32 v[130:131], v[114:115], s[4:5], v[66:67] op_sel_hi:[1,0,1]
	v_pk_fma_f32 v[132:133], v[116:117], s[4:5], v[68:69] op_sel_hi:[1,0,1]
	v_pk_fma_f32 v[134:135], v[118:119], s[4:5], v[70:71] op_sel_hi:[1,0,1]
	v_pk_fma_f32 v[136:137], v[120:121], s[4:5], v[72:73] op_sel_hi:[1,0,1]
	v_pk_fma_f32 v[138:139], v[122:123], s[4:5], v[74:75] op_sel_hi:[1,0,1]
	v_pk_fma_f32 v[140:141], v[124:125], s[4:5], v[76:77] op_sel_hi:[1,0,1]
	v_pk_fma_f32 v[142:143], v[126:127], s[4:5], v[78:79] op_sel_hi:[1,0,1]
	v_pk_fma_f32 v[144:145], v[128:129], s[4:5], v[80:81] op_sel_hi:[1,0,1]
	v_exp_f32_e32 v130, v130
	v_exp_f32_e32 v131, v131
	v_exp_f32_e32 v132, v132
	v_exp_f32_e32 v133, v133
	v_exp_f32_e32 v134, v134
	v_exp_f32_e32 v135, v135
	v_exp_f32_e32 v136, v136
	v_exp_f32_e32 v137, v137
	v_exp_f32_e32 v138, v138
	v_exp_f32_e32 v139, v139
	v_exp_f32_e32 v140, v140
	v_exp_f32_e32 v141, v141
	v_exp_f32_e32 v142, v142
	v_exp_f32_e32 v143, v143
	v_exp_f32_e32 v144, v144
	v_exp_f32_e32 v145, v145
	v_pk_add_f32 v[130:131], v[130:131], 1.0 op_sel_hi:[1,0]
	v_pk_add_f32 v[132:133], v[132:133], 1.0 op_sel_hi:[1,0]
	v_pk_add_f32 v[134:135], v[134:135], 1.0 op_sel_hi:[1,0]
	v_pk_add_f32 v[136:137], v[136:137], 1.0 op_sel_hi:[1,0]
	v_pk_add_f32 v[138:139], v[138:139], 1.0 op_sel_hi:[1,0]
	v_pk_add_f32 v[140:141], v[140:141], 1.0 op_sel_hi:[1,0]
	v_pk_add_f32 v[142:143], v[142:143], 1.0 op_sel_hi:[1,0]
	v_pk_add_f32 v[144:145], v[144:145], 1.0 op_sel_hi:[1,0]
	v_rcp_f32_e32 v130, v130
	v_rcp_f32_e32 v131, v131
	v_rcp_f32_e32 v132, v132
	v_rcp_f32_e32 v133, v133
	v_rcp_f32_e32 v134, v134
	v_rcp_f32_e32 v135, v135
	v_rcp_f32_e32 v136, v136
	v_rcp_f32_e32 v137, v137
	v_rcp_f32_e32 v138, v138
	v_rcp_f32_e32 v139, v139
	v_rcp_f32_e32 v140, v140
	v_rcp_f32_e32 v141, v141
	v_rcp_f32_e32 v142, v142
	v_rcp_f32_e32 v143, v143
	v_rcp_f32_e32 v144, v144
	v_rcp_f32_e32 v145, v145
	v_pk_fma_f32 v[130:131], v[130:131], 2.0, 1.0 op_sel_hi:[1,0,0] neg_lo:[1,0,0] neg_hi:[1,0,0]
	v_pk_fma_f32 v[132:133], v[132:133], 2.0, 1.0 op_sel_hi:[1,0,0] neg_lo:[1,0,0] neg_hi:[1,0,0]
	v_pk_fma_f32 v[134:135], v[134:135], 2.0, 1.0 op_sel_hi:[1,0,0] neg_lo:[1,0,0] neg_hi:[1,0,0]
	v_pk_fma_f32 v[136:137], v[136:137], 2.0, 1.0 op_sel_hi:[1,0,0] neg_lo:[1,0,0] neg_hi:[1,0,0]
	v_pk_fma_f32 v[138:139], v[138:139], 2.0, 1.0 op_sel_hi:[1,0,0] neg_lo:[1,0,0] neg_hi:[1,0,0]
	v_pk_fma_f32 v[140:141], v[140:141], 2.0, 1.0 op_sel_hi:[1,0,0] neg_lo:[1,0,0] neg_hi:[1,0,0]
	v_pk_fma_f32 v[142:143], v[142:143], 2.0, 1.0 op_sel_hi:[1,0,0] neg_lo:[1,0,0] neg_hi:[1,0,0]
	v_pk_fma_f32 v[144:145], v[144:145], 2.0, 1.0 op_sel_hi:[1,0,0] neg_lo:[1,0,0] neg_hi:[1,0,0]
	v_cvt_pk_f16_f32 v146, v130, v131
	v_cvt_pk_f16_f32 v147, v132, v133
	v_cvt_pk_f16_f32 v148, v134, v135
	v_cvt_pk_f16_f32 v149, v136, v137
	v_cvt_pk_f16_f32 v150, v138, v139
	v_cvt_pk_f16_f32 v151, v140, v141
	v_cvt_pk_f16_f32 v152, v142, v143
	v_cvt_pk_f16_f32 v153, v144, v145
	s_nop 1
	v_permlane32_swap_b32_e32 v146, v148
	v_permlane32_swap_b32_e32 v147, v149
	v_permlane32_swap_b32_e32 v150, v152
	v_permlane32_swap_b32_e32 v151, v153
	global_store_dwordx4 v157, v[146:149], s[32:33] sc1
	global_store_dwordx4 v157, v[150:153], s[32:33] offset:1024 sc1
	s_add_u32 s32, s32, 0x10000
	s_addc_u32 s33, s33, 0
	s_waitcnt lgkmcnt(0)
	v_mfma_f32_32x32x16_f16 v[114:129], v[82:85], v[50:53], 0
	v_mfma_f32_32x32x16_f16 v[114:129], v[86:89], v[54:57], v[114:129]
	v_mfma_f32_32x32x16_f16 v[114:129], v[90:93], v[58:61], v[114:129]
	v_mfma_f32_32x32x16_f16 v[114:129], v[94:97], v[62:65], v[114:129]
	v_pk_fma_f32 v[130:131], v[98:99], s[4:5], v[66:67] op_sel_hi:[1,0,1]
	v_pk_fma_f32 v[132:133], v[100:101], s[4:5], v[68:69] op_sel_hi:[1,0,1]
	v_pk_fma_f32 v[134:135], v[102:103], s[4:5], v[70:71] op_sel_hi:[1,0,1]
	v_pk_fma_f32 v[136:137], v[104:105], s[4:5], v[72:73] op_sel_hi:[1,0,1]
	v_pk_fma_f32 v[138:139], v[106:107], s[4:5], v[74:75] op_sel_hi:[1,0,1]
	v_pk_fma_f32 v[140:141], v[108:109], s[4:5], v[76:77] op_sel_hi:[1,0,1]
	v_pk_fma_f32 v[142:143], v[110:111], s[4:5], v[78:79] op_sel_hi:[1,0,1]
	v_pk_fma_f32 v[144:145], v[112:113], s[4:5], v[80:81] op_sel_hi:[1,0,1]
	v_exp_f32_e32 v130, v130
	v_exp_f32_e32 v131, v131
	v_exp_f32_e32 v132, v132
	v_exp_f32_e32 v133, v133
	v_exp_f32_e32 v134, v134
	v_exp_f32_e32 v135, v135
	v_exp_f32_e32 v136, v136
	v_exp_f32_e32 v137, v137
	v_exp_f32_e32 v138, v138
	v_exp_f32_e32 v139, v139
	v_exp_f32_e32 v140, v140
	v_exp_f32_e32 v141, v141
	v_exp_f32_e32 v142, v142
	v_exp_f32_e32 v143, v143
	v_exp_f32_e32 v144, v144
	v_exp_f32_e32 v145, v145
	v_pk_add_f32 v[130:131], v[130:131], 1.0 op_sel_hi:[1,0]
	v_pk_add_f32 v[132:133], v[132:133], 1.0 op_sel_hi:[1,0]
	v_pk_add_f32 v[134:135], v[134:135], 1.0 op_sel_hi:[1,0]
	v_pk_add_f32 v[136:137], v[136:137], 1.0 op_sel_hi:[1,0]
	v_pk_add_f32 v[138:139], v[138:139], 1.0 op_sel_hi:[1,0]
	v_pk_add_f32 v[140:141], v[140:141], 1.0 op_sel_hi:[1,0]
	v_pk_add_f32 v[142:143], v[142:143], 1.0 op_sel_hi:[1,0]
	v_pk_add_f32 v[144:145], v[144:145], 1.0 op_sel_hi:[1,0]
	v_rcp_f32_e32 v130, v130
	v_rcp_f32_e32 v131, v131
	v_rcp_f32_e32 v132, v132
	v_rcp_f32_e32 v133, v133
	v_rcp_f32_e32 v134, v134
	v_rcp_f32_e32 v135, v135
	v_rcp_f32_e32 v136, v136
	v_rcp_f32_e32 v137, v137
	v_rcp_f32_e32 v138, v138
	v_rcp_f32_e32 v139, v139
	v_rcp_f32_e32 v140, v140
	v_rcp_f32_e32 v141, v141
	v_rcp_f32_e32 v142, v142
	v_rcp_f32_e32 v143, v143
	v_rcp_f32_e32 v144, v144
	v_rcp_f32_e32 v145, v145
	v_pk_fma_f32 v[130:131], v[130:131], 2.0, 1.0 op_sel_hi:[1,0,0] neg_lo:[1,0,0] neg_hi:[1,0,0]
	v_pk_fma_f32 v[132:133], v[132:133], 2.0, 1.0 op_sel_hi:[1,0,0] neg_lo:[1,0,0] neg_hi:[1,0,0]
	v_pk_fma_f32 v[134:135], v[134:135], 2.0, 1.0 op_sel_hi:[1,0,0] neg_lo:[1,0,0] neg_hi:[1,0,0]
	v_pk_fma_f32 v[136:137], v[136:137], 2.0, 1.0 op_sel_hi:[1,0,0] neg_lo:[1,0,0] neg_hi:[1,0,0]
	v_pk_fma_f32 v[138:139], v[138:139], 2.0, 1.0 op_sel_hi:[1,0,0] neg_lo:[1,0,0] neg_hi:[1,0,0]
	v_pk_fma_f32 v[140:141], v[140:141], 2.0, 1.0 op_sel_hi:[1,0,0] neg_lo:[1,0,0] neg_hi:[1,0,0]
	v_pk_fma_f32 v[142:143], v[142:143], 2.0, 1.0 op_sel_hi:[1,0,0] neg_lo:[1,0,0] neg_hi:[1,0,0]
	v_pk_fma_f32 v[144:145], v[144:145], 2.0, 1.0 op_sel_hi:[1,0,0] neg_lo:[1,0,0] neg_hi:[1,0,0]
	v_cvt_pk_f16_f32 v146, v130, v131
	v_cvt_pk_f16_f32 v147, v132, v133
	v_cvt_pk_f16_f32 v148, v134, v135
	v_cvt_pk_f16_f32 v149, v136, v137
	v_cvt_pk_f16_f32 v150, v138, v139
	v_cvt_pk_f16_f32 v151, v140, v141
	v_cvt_pk_f16_f32 v152, v142, v143
	v_cvt_pk_f16_f32 v153, v144, v145
	s_nop 1
	v_permlane32_swap_b32_e32 v146, v148
	v_permlane32_swap_b32_e32 v147, v149
	v_permlane32_swap_b32_e32 v150, v152
	v_permlane32_swap_b32_e32 v151, v153
	global_store_dwordx4 v157, v[146:149], s[32:33] sc1
	global_store_dwordx4 v157, v[150:153], s[32:33] offset:1024 sc1
	s_add_u32 s32, s32, 0x10000
	s_addc_u32 s33, s33, 0
	v_pk_fma_f32 v[130:131], v[114:115], s[4:5], v[66:67] op_sel_hi:[1,0,1]
	v_pk_fma_f32 v[132:133], v[116:117], s[4:5], v[68:69] op_sel_hi:[1,0,1]
	v_pk_fma_f32 v[134:135], v[118:119], s[4:5], v[70:71] op_sel_hi:[1,0,1]
	v_pk_fma_f32 v[136:137], v[120:121], s[4:5], v[72:73] op_sel_hi:[1,0,1]
	v_pk_fma_f32 v[138:139], v[122:123], s[4:5], v[74:75] op_sel_hi:[1,0,1]
	v_pk_fma_f32 v[140:141], v[124:125], s[4:5], v[76:77] op_sel_hi:[1,0,1]
	v_pk_fma_f32 v[142:143], v[126:127], s[4:5], v[78:79] op_sel_hi:[1,0,1]
	v_pk_fma_f32 v[144:145], v[128:129], s[4:5], v[80:81] op_sel_hi:[1,0,1]
	v_exp_f32_e32 v130, v130
	v_exp_f32_e32 v131, v131
	v_exp_f32_e32 v132, v132
	v_exp_f32_e32 v133, v133
	v_exp_f32_e32 v134, v134
	v_exp_f32_e32 v135, v135
	v_exp_f32_e32 v136, v136
	v_exp_f32_e32 v137, v137
	v_exp_f32_e32 v138, v138
	v_exp_f32_e32 v139, v139
	v_exp_f32_e32 v140, v140
	v_exp_f32_e32 v141, v141
	v_exp_f32_e32 v142, v142
	v_exp_f32_e32 v143, v143
	v_exp_f32_e32 v144, v144
	v_exp_f32_e32 v145, v145
	v_pk_add_f32 v[130:131], v[130:131], 1.0 op_sel_hi:[1,0]
	v_pk_add_f32 v[132:133], v[132:133], 1.0 op_sel_hi:[1,0]
	v_pk_add_f32 v[134:135], v[134:135], 1.0 op_sel_hi:[1,0]
	v_pk_add_f32 v[136:137], v[136:137], 1.0 op_sel_hi:[1,0]
	v_pk_add_f32 v[138:139], v[138:139], 1.0 op_sel_hi:[1,0]
	v_pk_add_f32 v[140:141], v[140:141], 1.0 op_sel_hi:[1,0]
	v_pk_add_f32 v[142:143], v[142:143], 1.0 op_sel_hi:[1,0]
	v_pk_add_f32 v[144:145], v[144:145], 1.0 op_sel_hi:[1,0]
	v_rcp_f32_e32 v130, v130
	v_rcp_f32_e32 v131, v131
	v_rcp_f32_e32 v132, v132
	v_rcp_f32_e32 v133, v133
	v_rcp_f32_e32 v134, v134
	v_rcp_f32_e32 v135, v135
	v_rcp_f32_e32 v136, v136
	v_rcp_f32_e32 v137, v137
	v_rcp_f32_e32 v138, v138
	v_rcp_f32_e32 v139, v139
	v_rcp_f32_e32 v140, v140
	v_rcp_f32_e32 v141, v141
	v_rcp_f32_e32 v142, v142
	v_rcp_f32_e32 v143, v143
	v_rcp_f32_e32 v144, v144
	v_rcp_f32_e32 v145, v145
	v_pk_fma_f32 v[130:131], v[130:131], 2.0, 1.0 op_sel_hi:[1,0,0] neg_lo:[1,0,0] neg_hi:[1,0,0]
	v_pk_fma_f32 v[132:133], v[132:133], 2.0, 1.0 op_sel_hi:[1,0,0] neg_lo:[1,0,0] neg_hi:[1,0,0]
	v_pk_fma_f32 v[134:135], v[134:135], 2.0, 1.0 op_sel_hi:[1,0,0] neg_lo:[1,0,0] neg_hi:[1,0,0]
	v_pk_fma_f32 v[136:137], v[136:137], 2.0, 1.0 op_sel_hi:[1,0,0] neg_lo:[1,0,0] neg_hi:[1,0,0]
	v_pk_fma_f32 v[138:139], v[138:139], 2.0, 1.0 op_sel_hi:[1,0,0] neg_lo:[1,0,0] neg_hi:[1,0,0]
	v_pk_fma_f32 v[140:141], v[140:141], 2.0, 1.0 op_sel_hi:[1,0,0] neg_lo:[1,0,0] neg_hi:[1,0,0]
	v_pk_fma_f32 v[142:143], v[142:143], 2.0, 1.0 op_sel_hi:[1,0,0] neg_lo:[1,0,0] neg_hi:[1,0,0]
	v_pk_fma_f32 v[144:145], v[144:145], 2.0, 1.0 op_sel_hi:[1,0,0] neg_lo:[1,0,0] neg_hi:[1,0,0]
	v_cvt_pk_f16_f32 v146, v130, v131
	v_cvt_pk_f16_f32 v147, v132, v133
	v_cvt_pk_f16_f32 v148, v134, v135
	v_cvt_pk_f16_f32 v149, v136, v137
	v_cvt_pk_f16_f32 v150, v138, v139
	v_cvt_pk_f16_f32 v151, v140, v141
	v_cvt_pk_f16_f32 v152, v142, v143
	v_cvt_pk_f16_f32 v153, v144, v145
	s_nop 1
	v_permlane32_swap_b32_e32 v146, v148
	v_permlane32_swap_b32_e32 v147, v149
	v_permlane32_swap_b32_e32 v150, v152
	v_permlane32_swap_b32_e32 v151, v153
	global_store_dwordx4 v157, v[146:149], s[32:33] sc1
	global_store_dwordx4 v157, v[150:153], s[32:33] offset:1024 sc1
	s_waitcnt vmcnt(11)
	v_cvt_pk_f16_f32 v168, v168, v169
	v_cvt_pk_f16_f32 v169, v170, v171
	ds_write_b64 v164, v[168:169] offset:0
	s_waitcnt vmcnt(10)
	v_cvt_pk_f16_f32 v172, v172, v173
	v_cvt_pk_f16_f32 v173, v174, v175
	ds_write_b64 v164, v[172:173] offset:64
	s_waitcnt vmcnt(9)
	v_cvt_pk_f16_f32 v176, v176, v177
	v_cvt_pk_f16_f32 v177, v178, v179
	ds_write_b64 v164, v[176:177] offset:128
	s_waitcnt vmcnt(8)
	v_cvt_pk_f16_f32 v180, v180, v181
	v_cvt_pk_f16_f32 v181, v182, v183
	ds_write_b64 v164, v[180:181] offset:192
	s_waitcnt lgkmcnt(0)
	s_barrier
	ds_read_b128 v[2:5], v166
	ds_read_b128 v[6:9], v166 offset:32
	ds_read_u16 v10, v167 offset:0
	ds_read_u16 v11, v167 offset:272
	ds_read_u16 v12, v167 offset:544
	ds_read_u16 v13, v167 offset:816
	ds_read_u16 v14, v167 offset:1088
	ds_read_u16 v15, v167 offset:1360
	ds_read_u16 v16, v167 offset:1632
	ds_read_u16 v17, v167 offset:1904
	s_waitcnt lgkmcnt(8)
	global_store_dwordx4 v157, v[2:5], s[36:37] sc1
	global_store_dwordx4 v157, v[6:9], s[36:37] offset:1024 sc1
	s_waitcnt lgkmcnt(0)
	v_lshl_or_b32 v10, v11, 16, v10
	v_lshl_or_b32 v11, v13, 16, v12
	v_lshl_or_b32 v12, v15, 16, v14
	v_lshl_or_b32 v13, v17, 16, v16
	global_store_dwordx4 v157, v[10:13], s[38:39] sc1
	ds_read_u16 v18, v167 offset:4352
	ds_read_u16 v19, v167 offset:4624
	ds_read_u16 v20, v167 offset:4896
	ds_read_u16 v21, v167 offset:5168
	ds_read_u16 v22, v167 offset:5440
	ds_read_u16 v23, v167 offset:5712
	ds_read_u16 v24, v167 offset:5984
	ds_read_u16 v25, v167 offset:6256
	s_waitcnt lgkmcnt(0)
	v_lshl_or_b32 v18, v19, 16, v18
	v_lshl_or_b32 v19, v21, 16, v20
	v_lshl_or_b32 v20, v23, 16, v22
	v_lshl_or_b32 v21, v25, 16, v24
	global_store_dwordx4 v157, v[18:21], s[38:39] offset:1024 sc1
	s_endpgm
